# m2 + grid barrier L1 invalidate moved off the critical path (before polling / after generation bump)
# speedup vs baseline: 1.0050x; 1.0050x over previous
; __device__ __forceinline__ unsigned xb_ld(unsigned* p)              { return __hip_atomic_load(p, __ATOMIC_RELAXED, __HIP_MEMORY_SCOPE_AGENT); }
; __device__ __forceinline__ unsigned xb_add(unsigned* p, unsigned v) { return __hip_atomic_fetch_add(p, v, __ATOMIC_RELAXED, __HIP_MEMORY_SCOPE_AGENT); }
; #define XB_SPIN(cond, bar) do { unsigned _sp = 0; while (cond) { __builtin_amdgcn_s_sleep(1); \
;     if ((++_sp & 255u) == 0u) { if (xb_ld(&(bar)[XB_TMO])) break; if (_sp > XB_SPIN_CAP) { atomicAdd(&(bar)[XB_TMO], 1u); break; } } } } while (0)
; __device__ __forceinline__ void xcd_barrier(const XcdBarrier& b) {
;     ...
;         const unsigned old = xb_add(&bar[XB_XSUB(b.x)], 1u);
;         const unsigned gen = old / nloc;
;         if (old + 1u == (gen + 1u) * nloc) {
;             __builtin_amdgcn_fence(__ATOMIC_RELEASE, "agent");
;             asm volatile("s_waitcnt vmcnt(0)" ::: "memory");
;             const unsigned og = xb_add(&bar[XB_TOP], 1u);
;             const unsigned tg = og / nx;
;             if (og + 1u == (tg + 1u) * nx) xb_add(&bar[XB_TOPGEN], 1u);
;             else XB_SPIN(xb_ld(&bar[XB_TOPGEN]) == tg, bar);
;             __builtin_amdgcn_fence(__ATOMIC_ACQUIRE, "agent");
;             xb_add(&bar[XB_XGEN(b.x)], 1u);
;             asm volatile("s_waitcnt vmcnt(0)" ::: "memory");
;         } else {
;             XB_SPIN(xb_ld(&bar[XB_XGEN(b.x)]) == gen, bar);
.LBB0_59:
	s_or_b64 exec, exec, s[8:9]
	v_cvt_f32_u32_e32 v5, v3
	s_waitcnt vmcnt(0)
	v_readfirstlane_b32 s6, v4
	v_sub_u32_e32 v4, 0, v3
	v_rcp_iflag_f32_e32 v5, v5
	v_add_u32_e32 v6, s6, v2
	v_mul_f32_e32 v5, 0x4f7ffffe, v5
	v_cvt_u32_f32_e32 v5, v5
	v_mul_lo_u32 v2, v4, v5
	v_mul_hi_u32 v2, v5, v2
	v_add_u32_e32 v2, v5, v2
	v_mul_hi_u32 v2, v6, v2
	v_mul_lo_u32 v4, v2, v3
	v_sub_u32_e32 v4, v6, v4
	v_add_u32_e32 v5, 1, v2
	v_cmp_ge_u32_e32 vcc, v4, v3
	s_nop 1
	v_cndmask_b32_e32 v2, v2, v5, vcc
	v_sub_u32_e32 v5, v4, v3
	v_cndmask_b32_e32 v4, v4, v5, vcc
	v_add_u32_e32 v5, 1, v2
	v_cmp_ge_u32_e32 vcc, v4, v3
	v_add_u32_e32 v4, 1, v6
	s_nop 0
	v_cndmask_b32_e32 v2, v2, v5, vcc
	v_mul_lo_u32 v5, v3, v2
	v_add_u32_e32 v3, v5, v3
	v_cmp_ne_u32_e32 vcc, v4, v3
	s_and_saveexec_b64 s[6:7], vcc
	s_xor_b64 s[6:7], exec, s[6:7]
	s_cbranch_execz .LBB0_73
	s_waitcnt lgkmcnt(0)
	v_mov_b32_e32 v1, 0x2000
	buffer_inv sc1
	global_load_dword v1, v1, s[4:5] offset:1024 sc1
	s_add_u32 s12, s4, 0x2400
	s_addc_u32 s13, s5, 0
	s_waitcnt vmcnt(0)
	v_cmp_eq_u32_e32 vcc, v1, v2
	s_and_saveexec_b64 s[8:9], vcc
	s_cbranch_execz .LBB0_72
	s_add_u32 s10, s90, 0x4200
	s_addc_u32 s11, s91, 0
	s_mov_b32 s24, 1
	s_mov_b64 s[14:15], 0
	v_mov_b32_e32 v1, 0
	s_branch .LBB0_63

; __device__ __forceinline__ unsigned xb_ld(unsigned* p)              { return __hip_atomic_load(p, __ATOMIC_RELAXED, __HIP_MEMORY_SCOPE_AGENT); }
; #define XB_SPIN(cond, bar) do { unsigned _sp = 0; while (cond) { __builtin_amdgcn_s_sleep(1); \
;     if ((++_sp & 255u) == 0u) { if (xb_ld(&(bar)[XB_TMO])) break; if (_sp > XB_SPIN_CAP) { atomicAdd(&(bar)[XB_TMO], 1u); break; } } } } while (0)
; __device__ __forceinline__ void xcd_barrier(const XcdBarrier& b) {
;     ...
;             XB_SPIN(xb_ld(&bar[XB_XGEN(b.x)]) == gen, bar);
;             __builtin_amdgcn_fence(__ATOMIC_ACQUIRE, "agent");
;             asm volatile("s_waitcnt vmcnt(0)" ::: "memory");
.LBB0_72:
	s_or_b64 exec, exec, s[8:9]
	s_waitcnt vmcnt(0)
	s_waitcnt vmcnt(0)

; __device__ __forceinline__ unsigned xb_ld(unsigned* p)              { return __hip_atomic_load(p, __ATOMIC_RELAXED, __HIP_MEMORY_SCOPE_AGENT); }
; __device__ __forceinline__ unsigned xb_add(unsigned* p, unsigned v) { return __hip_atomic_fetch_add(p, v, __ATOMIC_RELAXED, __HIP_MEMORY_SCOPE_AGENT); }
; #define XB_SPIN(cond, bar) do { unsigned _sp = 0; while (cond) { __builtin_amdgcn_s_sleep(1); \
;     if ((++_sp & 255u) == 0u) { if (xb_ld(&(bar)[XB_TMO])) break; if (_sp > XB_SPIN_CAP) { atomicAdd(&(bar)[XB_TMO], 1u); break; } } } } while (0)
; __device__ __forceinline__ void xcd_barrier(const XcdBarrier& b) {
;     ...
;             const unsigned og = xb_add(&bar[XB_TOP], 1u);
;             const unsigned tg = og / nx;
;             if (og + 1u == (tg + 1u) * nx) xb_add(&bar[XB_TOPGEN], 1u);
;             else XB_SPIN(xb_ld(&bar[XB_TOPGEN]) == tg, bar);
;             __builtin_amdgcn_fence(__ATOMIC_ACQUIRE, "agent");
;             xb_add(&bar[XB_XGEN(b.x)], 1u);
;             asm volatile("s_waitcnt vmcnt(0)" ::: "memory");
.LBB0_90:
	s_or_b64 exec, exec, s[6:7]
	s_mov_b64 s[6:7], exec
	v_mbcnt_lo_u32_b32 v1, s6, 0
	v_mbcnt_hi_u32_b32 v1, s7, v1
	v_cmp_eq_u32_e32 vcc, 0, v1
	s_waitcnt vmcnt(0)
	s_and_saveexec_b64 s[8:9], vcc
	s_cbranch_execz .LBB0_92
	s_bcnt1_i32_b64 s6, s[6:7]
	v_mov_b32_e32 v1, 0x2000
	v_mov_b32_e32 v2, s6
	global_atomic_add v1, v2, s[4:5] offset:1024
.LBB0_92:
	s_or_b64 exec, exec, s[8:9]
	buffer_inv sc1
	s_waitcnt vmcnt(0)

; __device__ __forceinline__ unsigned xb_add(unsigned* p, unsigned v) { return __hip_atomic_fetch_add(p, v, __ATOMIC_RELAXED, __HIP_MEMORY_SCOPE_AGENT); }
; __device__ __forceinline__ void xcd_barrier(const XcdBarrier& b) {
;     ...
;             __builtin_amdgcn_fence(__ATOMIC_ACQUIRE, "agent");
;             xb_add(&bar[XB_XGEN(b.x)], 1u);
;             asm volatile("s_waitcnt vmcnt(0)" ::: "memory");
.LBB0_95:
	s_or_b64 exec, exec, s[4:5]
	buffer_inv sc1
	s_waitcnt vmcnt(0)

; __device__ __forceinline__ unsigned xb_ld(unsigned* p)              { return __hip_atomic_load(p, __ATOMIC_RELAXED, __HIP_MEMORY_SCOPE_AGENT); }
; __device__ __forceinline__ unsigned xb_add(unsigned* p, unsigned v) { return __hip_atomic_fetch_add(p, v, __ATOMIC_RELAXED, __HIP_MEMORY_SCOPE_AGENT); }
; #define XB_SPIN(cond, bar) do { unsigned _sp = 0; while (cond) { __builtin_amdgcn_s_sleep(1); \
;     if ((++_sp & 255u) == 0u) { if (xb_ld(&(bar)[XB_TMO])) break; if (_sp > XB_SPIN_CAP) { atomicAdd(&(bar)[XB_TMO], 1u); break; } } } } while (0)
; __device__ __forceinline__ void xcd_barrier(const XcdBarrier& b) {
;     ...
;         const unsigned old = xb_add(&bar[XB_XSUB(b.x)], 1u);
;         const unsigned gen = old / nloc;
;         if (old + 1u == (gen + 1u) * nloc) {
;             __builtin_amdgcn_fence(__ATOMIC_RELEASE, "agent");
;             asm volatile("s_waitcnt vmcnt(0)" ::: "memory");
;             const unsigned og = xb_add(&bar[XB_TOP], 1u);
;             const unsigned tg = og / nx;
;             if (og + 1u == (tg + 1u) * nx) xb_add(&bar[XB_TOPGEN], 1u);
;             else XB_SPIN(xb_ld(&bar[XB_TOPGEN]) == tg, bar);
;             __builtin_amdgcn_fence(__ATOMIC_ACQUIRE, "agent");
;             xb_add(&bar[XB_XGEN(b.x)], 1u);
;             asm volatile("s_waitcnt vmcnt(0)" ::: "memory");
;         } else {
;             XB_SPIN(xb_ld(&bar[XB_XGEN(b.x)]) == gen, bar);
.LBB0_195:
	s_or_b64 exec, exec, s[2:3]
	v_cvt_f32_u32_e32 v1, v4
	s_waitcnt vmcnt(0)
	v_readfirstlane_b32 s2, v5
	v_sub_u32_e32 v5, 0, v4
	v_rcp_iflag_f32_e32 v1, v1
	v_add_u32_e32 v6, s2, v3
	v_mul_f32_e32 v1, 0x4f7ffffe, v1
	v_cvt_u32_f32_e32 v1, v1
	v_mul_lo_u32 v3, v5, v1
	v_mul_hi_u32 v3, v1, v3
	v_add_u32_e32 v1, v1, v3
	v_mul_hi_u32 v1, v6, v1
	v_mul_lo_u32 v3, v1, v4
	v_sub_u32_e32 v3, v6, v3
	v_add_u32_e32 v5, 1, v1
	v_cmp_ge_u32_e32 vcc, v3, v4
	s_nop 1
	v_cndmask_b32_e32 v1, v1, v5, vcc
	v_sub_u32_e32 v5, v3, v4
	v_cndmask_b32_e32 v3, v3, v5, vcc
	v_add_u32_e32 v5, 1, v1
	v_cmp_ge_u32_e32 vcc, v3, v4
	s_nop 1
	v_cndmask_b32_e32 v3, v1, v5, vcc
	v_mul_lo_u32 v5, v4, v3
	v_add_u32_e32 v1, 1, v6
	v_add_u32_e32 v4, v5, v4
	v_cmp_ne_u32_e32 vcc, v1, v4
	s_and_saveexec_b64 s[2:3], vcc
	s_xor_b64 s[2:3], exec, s[2:3]
	s_cbranch_execz .LBB0_209
	v_readlane_b32 s4, v253, 57
	v_readlane_b32 s5, v253, 58
	s_nop 4
	buffer_inv sc1
	global_load_dword v1, v35, s[4:5] sc1
	s_waitcnt vmcnt(0)
	v_cmp_eq_u32_e32 vcc, v1, v3
	s_and_saveexec_b64 s[4:5], vcc
	s_cbranch_execz .LBB0_208
	s_mov_b32 s17, 1
	s_mov_b64 s[6:7], 0
	s_branch .LBB0_199

; __device__ __forceinline__ unsigned xb_ld(unsigned* p)              { return __hip_atomic_load(p, __ATOMIC_RELAXED, __HIP_MEMORY_SCOPE_AGENT); }
; #define XB_SPIN(cond, bar) do { unsigned _sp = 0; while (cond) { __builtin_amdgcn_s_sleep(1); \
;     if ((++_sp & 255u) == 0u) { if (xb_ld(&(bar)[XB_TMO])) break; if (_sp > XB_SPIN_CAP) { atomicAdd(&(bar)[XB_TMO], 1u); break; } } } } while (0)
; __device__ __forceinline__ void xcd_barrier(const XcdBarrier& b) {
;     ...
;             XB_SPIN(xb_ld(&bar[XB_XGEN(b.x)]) == gen, bar);
;             __builtin_amdgcn_fence(__ATOMIC_ACQUIRE, "agent");
;             asm volatile("s_waitcnt vmcnt(0)" ::: "memory");
.LBB0_208:
	s_or_b64 exec, exec, s[4:5]
	s_waitcnt vmcnt(0) lgkmcnt(0)
	s_waitcnt vmcnt(0)

; __device__ __forceinline__ unsigned xb_ld(unsigned* p)              { return __hip_atomic_load(p, __ATOMIC_RELAXED, __HIP_MEMORY_SCOPE_AGENT); }
; __device__ __forceinline__ unsigned xb_add(unsigned* p, unsigned v) { return __hip_atomic_fetch_add(p, v, __ATOMIC_RELAXED, __HIP_MEMORY_SCOPE_AGENT); }
; #define XB_SPIN(cond, bar) do { unsigned _sp = 0; while (cond) { __builtin_amdgcn_s_sleep(1); \
;     if ((++_sp & 255u) == 0u) { if (xb_ld(&(bar)[XB_TMO])) break; if (_sp > XB_SPIN_CAP) { atomicAdd(&(bar)[XB_TMO], 1u); break; } } } } while (0)
; __device__ __forceinline__ void xcd_barrier(const XcdBarrier& b) {
;     ...
;             if (og + 1u == (tg + 1u) * nx) xb_add(&bar[XB_TOPGEN], 1u);
;             else XB_SPIN(xb_ld(&bar[XB_TOPGEN]) == tg, bar);
;             __builtin_amdgcn_fence(__ATOMIC_ACQUIRE, "agent");
;             xb_add(&bar[XB_XGEN(b.x)], 1u);
.LBB0_226:
	s_or_b64 exec, exec, s[2:3]
	s_mov_b64 s[2:3], exec
	v_mbcnt_lo_u32_b32 v1, s2, 0
	v_mbcnt_hi_u32_b32 v1, s3, v1
	v_cmp_eq_u32_e32 vcc, 0, v1
	s_waitcnt vmcnt(0)
	s_and_saveexec_b64 s[4:5], vcc
	s_cbranch_execz .LBB0_228
	s_bcnt1_i32_b64 s2, s[2:3]
	v_mov_b32_e32 v1, s2
	v_readlane_b32 s2, v253, 57
	v_readlane_b32 s3, v253, 58
	s_nop 4
	global_atomic_add v35, v1, s[2:3]

; __device__ __forceinline__ unsigned xb_ld(unsigned* p)              { return __hip_atomic_load(p, __ATOMIC_RELAXED, __HIP_MEMORY_SCOPE_AGENT); }
; __device__ __forceinline__ unsigned xb_add(unsigned* p, unsigned v) { return __hip_atomic_fetch_add(p, v, __ATOMIC_RELAXED, __HIP_MEMORY_SCOPE_AGENT); }
; #define XB_SPIN(cond, bar) do { unsigned _sp = 0; while (cond) { __builtin_amdgcn_s_sleep(1); \
;     if ((++_sp & 255u) == 0u) { if (xb_ld(&(bar)[XB_TMO])) break; if (_sp > XB_SPIN_CAP) { atomicAdd(&(bar)[XB_TMO], 1u); break; } } } } while (0)
; __device__ __forceinline__ void xcd_barrier(const XcdBarrier& b) {
;     ...
;         const unsigned old = xb_add(&bar[XB_XSUB(b.x)], 1u);
;         const unsigned gen = old / nloc;
;         if (old + 1u == (gen + 1u) * nloc) {
;             __builtin_amdgcn_fence(__ATOMIC_RELEASE, "agent");
;             asm volatile("s_waitcnt vmcnt(0)" ::: "memory");
;             const unsigned og = xb_add(&bar[XB_TOP], 1u);
;             const unsigned tg = og / nx;
;             if (og + 1u == (tg + 1u) * nx) xb_add(&bar[XB_TOPGEN], 1u);
;             else XB_SPIN(xb_ld(&bar[XB_TOPGEN]) == tg, bar);
;             __builtin_amdgcn_fence(__ATOMIC_ACQUIRE, "agent");
;             xb_add(&bar[XB_XGEN(b.x)], 1u);
;             asm volatile("s_waitcnt vmcnt(0)" ::: "memory");
;         } else {
;             XB_SPIN(xb_ld(&bar[XB_XGEN(b.x)]) == gen, bar);
.LBB0_390:
	s_or_b64 exec, exec, s[2:3]
	v_cvt_f32_u32_e32 v1, v4
	s_waitcnt vmcnt(0)
	v_readfirstlane_b32 s2, v5
	v_sub_u32_e32 v5, 0, v4
	v_rcp_iflag_f32_e32 v1, v1
	v_add_u32_e32 v6, s2, v3
	v_mul_f32_e32 v1, 0x4f7ffffe, v1
	v_cvt_u32_f32_e32 v1, v1
	v_mul_lo_u32 v3, v5, v1
	v_mul_hi_u32 v3, v1, v3
	v_add_u32_e32 v1, v1, v3
	v_mul_hi_u32 v1, v6, v1
	v_mul_lo_u32 v3, v1, v4
	v_sub_u32_e32 v3, v6, v3
	v_add_u32_e32 v5, 1, v1
	v_cmp_ge_u32_e32 vcc, v3, v4
	s_nop 1
	v_cndmask_b32_e32 v1, v1, v5, vcc
	v_sub_u32_e32 v5, v3, v4
	v_cndmask_b32_e32 v3, v3, v5, vcc
	v_add_u32_e32 v5, 1, v1
	v_cmp_ge_u32_e32 vcc, v3, v4
	s_nop 1
	v_cndmask_b32_e32 v3, v1, v5, vcc
	v_mul_lo_u32 v5, v4, v3
	v_add_u32_e32 v1, 1, v6
	v_add_u32_e32 v4, v5, v4
	v_cmp_ne_u32_e32 vcc, v1, v4
	s_and_saveexec_b64 s[2:3], vcc
	s_xor_b64 s[2:3], exec, s[2:3]
	s_cbranch_execz .LBB0_404
	v_readlane_b32 s4, v253, 57
	v_readlane_b32 s5, v253, 58
	s_nop 4
	buffer_inv sc1
	global_load_dword v1, v35, s[4:5] sc1
	s_waitcnt vmcnt(0)
	v_cmp_eq_u32_e32 vcc, v1, v3
	s_and_saveexec_b64 s[4:5], vcc
	s_cbranch_execz .LBB0_403
	s_mov_b32 s16, 1
	s_mov_b64 s[6:7], 0
	s_branch .LBB0_394

; __device__ __forceinline__ unsigned xb_ld(unsigned* p)              { return __hip_atomic_load(p, __ATOMIC_RELAXED, __HIP_MEMORY_SCOPE_AGENT); }
; __device__ __forceinline__ unsigned xb_add(unsigned* p, unsigned v) { return __hip_atomic_fetch_add(p, v, __ATOMIC_RELAXED, __HIP_MEMORY_SCOPE_AGENT); }
; #define XB_SPIN(cond, bar) do { unsigned _sp = 0; while (cond) { __builtin_amdgcn_s_sleep(1); \
;     if ((++_sp & 255u) == 0u) { if (xb_ld(&(bar)[XB_TMO])) break; if (_sp > XB_SPIN_CAP) { atomicAdd(&(bar)[XB_TMO], 1u); break; } } } } while (0)
; __device__ __forceinline__ void xcd_barrier(const XcdBarrier& b) {
;     ...
;             if (og + 1u == (tg + 1u) * nx) xb_add(&bar[XB_TOPGEN], 1u);
;             else XB_SPIN(xb_ld(&bar[XB_TOPGEN]) == tg, bar);
;             __builtin_amdgcn_fence(__ATOMIC_ACQUIRE, "agent");
;             xb_add(&bar[XB_XGEN(b.x)], 1u);
.LBB0_1441:
	s_or_b64 exec, exec, s[2:3]
	s_mov_b64 s[2:3], exec
	v_mbcnt_lo_u32_b32 v1, s2, 0
	v_mbcnt_hi_u32_b32 v1, s3, v1
	v_cmp_eq_u32_e32 vcc, 0, v1
	s_waitcnt vmcnt(0)
	s_and_saveexec_b64 s[4:5], vcc
	s_cbranch_execnz .LBB0_1442
	s_getpc_b64 s[98:99]
